# baseline (speedup 1.0000x reference)
_Z10agg_kernelPKDF16_PKiS2_S2_PKfS2_PDF16_Pfi:
	s_load_dwordx8 s[12:19], s[0:1], 0x0
	s_lshl_b32 s4, s2, 1
	s_ashr_i32 s5, s4, 31
	s_lshl_b64 s[4:5], s[4:5], 2
	v_and_b32_e32 v1, 63, v0
	s_waitcnt lgkmcnt(0)
	s_add_u32 s20, s16, s4
	s_addc_u32 s21, s17, s5
	s_load_dwordx2 s[16:17], s[20:21], 0x0
	s_load_dwordx8 s[4:11], s[0:1], 0x20
	v_readfirstlane_b32 s3, v0
	v_lshlrev_b32_e32 v2, 2, v1
	s_lshr_b32 s3, s3, 6
	s_waitcnt lgkmcnt(0)
	s_ashr_i32 s21, s16, 31
	s_mov_b32 s20, s16
	global_load_dword v3, v2, s[6:7]
	global_load_dword v4, v2, s[6:7] offset:256
	global_load_dword v6, v2, s[6:7] offset:512
	global_load_dword v5, v2, s[6:7] offset:768
	s_lshl_b64 s[6:7], s[20:21], 2
	s_add_u32 s6, s14, s6
	s_addc_u32 s7, s15, s7
	s_add_i32 s21, s17, 15
	s_ashr_i32 s21, s21, 4
	s_max_i32 s20, s21, 1
	s_add_i32 s20, s20, -1
	s_min_u32 s14, s3, s20
	s_bfe_u32 s44, s2, 0x10002
	s_mul_i32 s45, s44, s20
	s_lshl_b32 s44, s44, 1
	s_sub_i32 s44, 1, s44
	s_mul_i32 s14, s14, s44
	s_add_i32 s14, s14, s45
	s_lshl_b32 s30, s14, 4
	v_mov_b32_e32 v59, 0x30e0000
	v_bfe_u32 v2, v0, 4, 2
	v_lshlrev_b32_e32 v7, 2, v0
	s_lshl_b32 s14, s14, 6
	v_and_or_b32 v18, v7, 12, v2
	s_add_u32 s14, s6, s14
	s_addc_u32 s15, s7, 0
	v_lshlrev_b32_e32 v2, 2, v18
	global_load_dword v2, v2, s[14:15]
	v_lshlrev_b32_e32 v20, 2, v18
	v_mov_b32_e32 v8, 0
	v_mov_b32_e32 v9, 0
	v_mov_b32_e32 v10, 0
	v_mov_b32_e32 v11, 0
	v_lshlrev_b32_e32 v12, 4, v0
	v_add_u32_e32 v13, 0x10000, v12
	ds_write_b128 v12, v[8:11]
	ds_write_b128 v12, v[8:11] offset:16384
	ds_write_b128 v12, v[8:11] offset:32768
	ds_write_b128 v12, v[8:11] offset:49152
	ds_write_b128 v13, v[8:11]
	ds_write_b128 v13, v[8:11] offset:16384
	ds_write_b128 v13, v[8:11] offset:32768
	v_cmp_gt_u32_e32 vcc, 0x28c, v0
	s_and_saveexec_b64 s[14:15], vcc
	ds_write_b128 v13, v[8:11] offset:49152
	s_or_b64 exec, exec, s[14:15]
	s_waitcnt vmcnt(2)
	v_max3_i32 v3, v3, v4, v6
	v_mbcnt_lo_u32_b32 v4, -1, 0
	v_mbcnt_hi_u32_b32 v4, -1, v4
	v_and_b32_e32 v25, 64, v4
	s_waitcnt vmcnt(1)
	v_max3_i32 v3, v3, v5, 0
	v_add_u32_e32 v5, 64, v25
	v_xor_b32_e32 v6, 1, v4
	v_cmp_lt_i32_e32 vcc, v6, v5
	s_load_dword s16, s[0:1], 0x40
	s_mul_i32 s14, s2, 0x187
	v_cndmask_b32_e32 v6, v4, v6, vcc
	v_lshlrev_b32_e32 v6, 2, v6
	ds_bpermute_b32 v6, v6, v3
	s_waitcnt lgkmcnt(0)
	s_sub_i32 s15, s16, s14
	s_movk_i32 s0, 0x73
	s_cmp_gt_i32 s21, s3
	s_cselect_b64 s[22:23], -1, 0
	v_max_i32_e32 v3, v3, v6
	v_xor_b32_e32 v6, 2, v4
	v_cmp_lt_i32_e32 vcc, v6, v5
	v_mov_b32_e32 v29, 0
	v_mov_b32_e32 v27, 0
	v_cndmask_b32_e32 v6, v4, v6, vcc
	v_lshlrev_b32_e32 v6, 2, v6
	ds_bpermute_b32 v6, v6, v3
	v_mov_b32_e32 v28, 0
	v_mov_b32_e32 v26, 0
	v_mov_b32_e32 v21, 0
	s_waitcnt lgkmcnt(0)
	v_max_i32_e32 v3, v3, v6
	v_xor_b32_e32 v6, 4, v4
	v_cmp_lt_i32_e32 vcc, v6, v5
	v_cndmask_b32_e32 v6, v4, v6, vcc
	v_lshlrev_b32_e32 v6, 2, v6
	ds_bpermute_b32 v6, v6, v3
	s_waitcnt lgkmcnt(0)
	s_barrier
	v_max_i32_e32 v3, v3, v6
	v_xor_b32_e32 v6, 8, v4
	v_cmp_lt_i32_e32 vcc, v6, v5
	s_nop 1
	v_cndmask_b32_e32 v6, v4, v6, vcc
	v_lshlrev_b32_e32 v60, 2, v6
	ds_bpermute_b32 v6, v60, v3
	s_waitcnt lgkmcnt(0)
	v_max_i32_e32 v3, v3, v6
	v_xor_b32_e32 v6, 16, v4
	v_cmp_lt_i32_e32 vcc, v6, v5
	s_nop 1
	v_cndmask_b32_e32 v6, v4, v6, vcc
	v_lshlrev_b32_e32 v61, 2, v6
	ds_bpermute_b32 v6, v61, v3
	s_waitcnt lgkmcnt(0)
	v_max_i32_e32 v3, v3, v6
	v_xor_b32_e32 v6, 32, v4
	v_cmp_lt_i32_e32 vcc, v6, v5
	v_and_b32_e32 v5, 15, v0
	v_lshlrev_b32_e32 v24, 4, v5
	v_cndmask_b32_e32 v4, v4, v6, vcc
	v_lshlrev_b32_e32 v66, 2, v4
	ds_bpermute_b32 v4, v66, v3
	v_lshlrev_b32_e32 v23, 2, v5
	s_waitcnt lgkmcnt(0)
	v_max_i32_e32 v3, v3, v4
	v_lshrrev_b32_e32 v3, 23, v3
	v_mov_b32_e32 v4, 0x8b
	v_med3_u32 v3, v3, s0, v4
	s_sub_i32 s0, s21, s3
	s_add_i32 s0, s0, 15
	s_cmp_gt_u32 s0, 15
	s_cselect_b64 s[24:25], -1, 0
	v_lshlrev_b32_e32 v19, 23, v3
	s_and_b64 s[22:23], s[22:23], s[24:25]
	v_sub_u32_e32 v22, 0x84800000, v19
	s_waitcnt vmcnt(0)
	v_add_u32_e32 v33, s30, v18
	v_cmp_gt_i32_e64 s[28:29], s17, v33
	s_nop 1
	v_cndmask_b32_e64 v2, v59, v2, s[28:29]
	s_nop 1
	v_mov_b32_dpp v29, v2 row_newbcast:0 row_mask:0xf bank_mask:0xf
	v_mov_b32_dpp v27, v2 row_newbcast:1 row_mask:0xf bank_mask:0xf
	v_mov_b32_dpp v28, v2 row_newbcast:2 row_mask:0xf bank_mask:0xf
	v_mov_b32_dpp v26, v2 row_newbcast:3 row_mask:0xf bank_mask:0xf
	s_add_i32 s49, s16, -1
	v_lshrrev_b32_e32 v30, 3, v0
	v_add_u32_e32 v30, s14, v30
	v_add_u32_e32 v31, 0, v30
	v_min_i32_e32 v31, s49, v31
	v_lshlrev_b32_e32 v31, 2, v31
	global_load_dword v62, v31, s[4:5]
	global_load_dword v63, v31, s[18:19]
	v_add_u32_e32 v31, 128, v30
	v_min_i32_e32 v31, s49, v31
	v_lshlrev_b32_e32 v31, 2, v31
	global_load_dword v64, v31, s[4:5]
	global_load_dword v65, v31, s[18:19]
	v_add_u32_e32 v31, 256, v30
	v_min_i32_e32 v31, s49, v31
	v_lshlrev_b32_e32 v31, 2, v31
	global_load_dword v67, v31, s[4:5]
	global_load_dword v68, v31, s[18:19]
	v_add_u32_e32 v31, 384, v30
	v_min_i32_e32 v31, s49, v31
	v_lshlrev_b32_e32 v31, 2, v31
	global_load_dword v69, v31, s[4:5]
	global_load_dword v58, v31, s[18:19]
	s_and_b64 vcc, exec, s[22:23]
	s_cbranch_vccz .LBB2_5
	s_lshr_b32 s21, s0, 4
	s_mov_b32 s1, 0
	s_mov_b32 s22, 0x1ffff00
	s_mov_b32 s23, 0x4b400000
	v_lshl_add_u64 v[20:21], s[6:7], 0, v[20:21]
	s_add_i32 s0, s3, 16
	s_mov_b32 s24, s0
	s_min_i32 s24, s24, s20
	s_mul_i32 s24, s24, s44
	s_add_i32 s24, s24, s45
	s_lshl_b32 s24, s24, 4
	s_ashr_i32 s25, s24, 31
	v_lshl_add_u64 v[32:33], s[24:25], 2, v[20:21]
	global_load_dword v30, v[32:33], off
	v_lshlrev_b32_e32 v35, 8, v29
	v_and_or_b32 v35, v35, s22, v24
	global_load_dwordx4 v[2:5], v35, s[12:13]
	v_lshlrev_b32_e32 v35, 8, v27
	v_and_or_b32 v35, v35, s22, v24
	global_load_dwordx4 v[6:9], v35, s[12:13]
	v_lshlrev_b32_e32 v35, 8, v28
	v_and_or_b32 v35, v35, s22, v24
	global_load_dwordx4 v[10:13], v35, s[12:13]
	v_lshlrev_b32_e32 v35, 8, v26
	v_and_or_b32 v35, v35, s22, v24
	global_load_dwordx4 v[14:17], v35, s[12:13]

.LBB2_15:
	v_lshrrev_b32_e32 v43, 3, v0
	s_waitcnt vmcnt(0)
	v_add_u32_e32 v2, s14, v43
	s_add_i32 s16, s16, -1
	v_add_u32_e32 v3, 0x80, v2
	v_min_i32_e32 v4, s16, v3
	v_ashrrev_i32_e32 v5, 31, v4
	v_lshlrev_b64 v[6:7], 2, v[4:5]
	v_lshl_add_u64 v[4:5], s[4:5], 0, v[6:7]
	v_lshl_add_u64 v[6:7], s[18:19], 0, v[6:7]
	v_add_u32_e32 v3, 0x100, v2
	v_mov_b32_e32 v4, v64
	v_mov_b32_e32 v38, 0
	v_mov_b32_e32 v5, v65
	v_min_i32_e32 v6, s16, v3
	v_ashrrev_i32_e32 v7, 31, v6
	v_lshlrev_b64 v[6:7], 2, v[6:7]
	v_lshl_add_u64 v[8:9], s[4:5], 0, v[6:7]
	v_lshl_add_u64 v[6:7], s[18:19], 0, v[6:7]
	v_add_u32_e32 v3, 0x180, v2
	v_mov_b32_e32 v49, v68
	v_min_i32_e32 v6, s16, v3
	v_ashrrev_i32_e32 v7, 31, v6
	v_lshlrev_b64 v[6:7], 2, v[6:7]
	v_mov_b32_e32 v48, v67
	v_lshl_add_u64 v[8:9], s[4:5], 0, v[6:7]
	v_lshl_add_u64 v[6:7], s[18:19], 0, v[6:7]
	v_mov_b32_e32 v44, v69
	v_mov_b32_e32 v46, v58
	v_lshlrev_b32_e32 v3, 3, v0
	v_and_b32_e32 v42, 56, v3
	v_add_u32_e32 v45, 0xfa800000, v19
	v_lshlrev_b32_e32 v47, 2, v42
	v_cmp_gt_i32_e32 vcc, s15, v43
	v_mov_b32_e32 v39, 0
	v_mov_b32_e32 v34, 0
	v_mov_b32_e32 v35, v38
	v_mov_b32_e32 v30, v38
	v_mov_b32_e32 v31, v38
	v_mov_b32_e32 v24, v38
	v_mov_b32_e32 v25, v38
	v_mov_b32_e32 v20, v38
	v_mov_b32_e32 v21, v38
	v_mov_b32_e32 v16, v38
	v_mov_b32_e32 v17, v38
	v_mov_b32_e32 v14, v38
	v_mov_b32_e32 v15, v38
	v_mov_b32_e32 v10, v38
	v_mov_b32_e32 v11, v38
	v_mov_b32_e32 v40, 0
	v_mov_b32_e32 v41, 0
	v_mov_b32_e32 v36, 0
	v_mov_b32_e32 v37, v38
	v_mov_b32_e32 v32, v38
	v_mov_b32_e32 v33, v38
	v_mov_b32_e32 v26, v38
	v_mov_b32_e32 v27, v38
	v_mov_b32_e32 v28, v38
	v_mov_b32_e32 v29, v38
	v_mov_b32_e32 v22, v38
	v_mov_b32_e32 v23, v38
	v_mov_b32_e32 v18, v38
	v_mov_b32_e32 v19, v38
	v_mov_b32_e32 v12, v38
	v_mov_b32_e32 v13, v38
	s_waitcnt lgkmcnt(0)
	s_barrier
	s_and_saveexec_b64 s[0:1], vcc
	s_cbranch_execz .LBB2_17
	v_min_i32_e32 v6, s16, v2
	v_ashrrev_i32_e32 v7, 31, v6
	v_lshlrev_b64 v[6:7], 2, v[6:7]
	v_lshl_add_u64 v[8:9], s[4:5], 0, v[6:7]
	v_lshl_add_u64 v[6:7], s[18:19], 0, v[6:7]
	v_mov_b32_e32 v23, v63
	v_mov_b32_e32 v22, v62
	s_movk_i32 s5, 0x140
	v_mad_u32_u24 v10, v43, s5, v47
	ds_read_b128 v[6:9], v10
	ds_read_b128 v[10:13], v10 offset:16
	v_ashrrev_i32_e32 v3, 31, v2
	v_lshlrev_b64 v[2:3], 8, v[2:3]
	v_lshlrev_b32_e32 v14, 1, v42
	v_mov_b32_e32 v15, 0
	v_lshl_add_u64 v[2:3], s[8:9], 0, v[2:3]
	v_lshl_add_u64 v[2:3], v[2:3], 0, v[14:15]
	s_waitcnt lgkmcnt(1)
	v_cvt_f32_i32_sdwa v15, sext(v7) dst_sel:DWORD dst_unused:UNUSED_PAD src0_sel:WORD_0
	v_cvt_f32_i32_sdwa v14, sext(v6) dst_sel:DWORD dst_unused:UNUSED_PAD src0_sel:WORD_0
	v_cvt_f32_i32_sdwa v17, sext(v9) dst_sel:DWORD dst_unused:UNUSED_PAD src0_sel:WORD_0
	v_cvt_f32_i32_sdwa v16, sext(v8) dst_sel:DWORD dst_unused:UNUSED_PAD src0_sel:WORD_0
	s_waitcnt lgkmcnt(0)
	v_cvt_f32_i32_sdwa v19, sext(v11) dst_sel:DWORD dst_unused:UNUSED_PAD src0_sel:WORD_0
	v_cvt_f32_i32_sdwa v18, sext(v10) dst_sel:DWORD dst_unused:UNUSED_PAD src0_sel:WORD_0
	s_mov_b32 s4, 0xb4c00000
	v_cvt_f32_i32_sdwa v21, sext(v13) dst_sel:DWORD dst_unused:UNUSED_PAD src0_sel:WORD_0
	v_cvt_f32_i32_sdwa v20, sext(v12) dst_sel:DWORD dst_unused:UNUSED_PAD src0_sel:WORD_0
	s_waitcnt vmcnt(1)
	v_mul_lo_u32 v26, v23, s4
	s_waitcnt vmcnt(0)
	v_mul_f32_e32 v28, v22, v45
	v_add_u32_e32 v29, v6, v26
	v_add_u32_e32 v34, v7, v26
	v_add_u32_e32 v35, v8, v26
	v_add_u32_e32 v38, v9, v26
	v_add_u32_e32 v39, v10, v26
	v_add_u32_e32 v52, v11, v26
	v_add_u32_e32 v53, v12, v26
	v_add_u32_e32 v54, v13, v26
	v_pk_mul_f32 v[22:23], v[28:29], v[14:15] op_sel_hi:[0,1]
	v_pk_mul_f32 v[24:25], v[28:29], v[16:17] op_sel_hi:[0,1]
	v_pk_mul_f32 v[30:31], v[28:29], v[18:19] op_sel_hi:[0,1]
	v_pk_fma_f32 v[32:33], v[28:29], v[18:19], 0 op_sel_hi:[0,1,0]
	v_pk_fma_f32 v[36:37], v[28:29], v[16:17], 0 op_sel_hi:[0,1,0]
	v_pk_fma_f32 v[40:41], v[28:29], v[14:15], 0 op_sel_hi:[0,1,0]
	v_sub_u32_sdwa v14, v34, sext(v7) dst_sel:DWORD dst_unused:UNUSED_PAD src0_sel:DWORD src1_sel:WORD_0
	v_sub_u32_sdwa v15, v29, sext(v6) dst_sel:DWORD dst_unused:UNUSED_PAD src0_sel:DWORD src1_sel:WORD_0
	v_sub_u32_sdwa v16, v38, sext(v9) dst_sel:DWORD dst_unused:UNUSED_PAD src0_sel:DWORD src1_sel:WORD_0
	v_sub_u32_sdwa v17, v35, sext(v8) dst_sel:DWORD dst_unused:UNUSED_PAD src0_sel:DWORD src1_sel:WORD_0
	v_sub_u32_sdwa v18, v52, sext(v11) dst_sel:DWORD dst_unused:UNUSED_PAD src0_sel:DWORD src1_sel:WORD_0
	v_sub_u32_sdwa v19, v39, sext(v10) dst_sel:DWORD dst_unused:UNUSED_PAD src0_sel:DWORD src1_sel:WORD_0
	v_sub_u32_sdwa v13, v54, sext(v13) dst_sel:DWORD dst_unused:UNUSED_PAD src0_sel:DWORD src1_sel:WORD_0
	v_sub_u32_sdwa v12, v53, sext(v12) dst_sel:DWORD dst_unused:UNUSED_PAD src0_sel:DWORD src1_sel:WORD_0
	v_cvt_f32_i32_sdwa v11, sext(v14) dst_sel:DWORD dst_unused:UNUSED_PAD src0_sel:WORD_1
	v_cvt_f32_i32_sdwa v10, sext(v15) dst_sel:DWORD dst_unused:UNUSED_PAD src0_sel:WORD_1
	v_cvt_f32_i32_sdwa v15, sext(v16) dst_sel:DWORD dst_unused:UNUSED_PAD src0_sel:WORD_1
	v_cvt_f32_i32_sdwa v14, sext(v17) dst_sel:DWORD dst_unused:UNUSED_PAD src0_sel:WORD_1
	v_cvt_f32_i32_sdwa v17, sext(v18) dst_sel:DWORD dst_unused:UNUSED_PAD src0_sel:WORD_1
	v_cvt_f32_i32_sdwa v16, sext(v19) dst_sel:DWORD dst_unused:UNUSED_PAD src0_sel:WORD_1
	v_cvt_f32_i32_sdwa v13, sext(v13) dst_sel:DWORD dst_unused:UNUSED_PAD src0_sel:WORD_1
	v_cvt_f32_i32_sdwa v12, sext(v12) dst_sel:DWORD dst_unused:UNUSED_PAD src0_sel:WORD_1
	v_pk_mul_f32 v[50:51], v[28:29], v[20:21] op_sel_hi:[0,1]
	v_pk_fma_f32 v[26:27], v[28:29], v[20:21], 0 op_sel_hi:[0,1,0]
	v_pk_mul_f32 v[20:21], v[28:29], v[10:11] op_sel_hi:[0,1]
	v_pk_mul_f32 v[54:55], v[28:29], v[14:15] op_sel_hi:[0,1]
	v_pk_mul_f32 v[56:57], v[28:29], v[16:17] op_sel_hi:[0,1]
	v_pk_mul_f32 v[58:59], v[28:29], v[12:13] op_sel_hi:[0,1]
	v_cvt_pk_f16_f32 v6, v22, v23
	v_cvt_pk_f16_f32 v7, v24, v25
	v_cvt_pk_f16_f32 v8, v30, v31
	v_cvt_pk_f16_f32 v9, v50, v51
	v_pk_mul_f32 v[38:39], v[22:23], v[22:23]
	v_pk_mul_f32 v[34:35], v[24:25], v[24:25]
	v_pk_mul_f32 v[30:31], v[30:31], v[30:31]
	v_pk_mul_f32 v[24:25], v[50:51], v[50:51]
	v_pk_fma_f32 v[12:13], v[28:29], v[12:13], 0 op_sel_hi:[0,1,0]
	v_pk_fma_f32 v[18:19], v[28:29], v[16:17], 0 op_sel_hi:[0,1,0]
	v_pk_fma_f32 v[22:23], v[28:29], v[14:15], 0 op_sel_hi:[0,1,0]
	v_pk_fma_f32 v[28:29], v[28:29], v[10:11], 0 op_sel_hi:[0,1,0]
	v_cvt_pk_f16_f32 v50, v20, v21
	v_pk_mul_f32 v[20:21], v[20:21], v[20:21]
	v_pk_mul_f32 v[16:17], v[54:55], v[54:55]
	v_pk_mul_f32 v[14:15], v[56:57], v[56:57]
	v_pk_mul_f32 v[10:11], v[58:59], v[58:59]
	v_cvt_pk_f16_f32 v51, v54, v55
	v_cvt_pk_f16_f32 v52, v56, v57
	v_cvt_pk_f16_f32 v53, v58, v59
	global_store_dwordx4 v[2:3], v[6:9], off sc1
	global_store_dwordx4 v[2:3], v[50:53], off offset:128 sc1
